# attn: per-workgroup start skew ((blockIdx>>3)&7 x ~0.1us) to de-synchronise the chip-wide A-store bursts
# speedup vs baseline: 1.0037x; 1.0037x over previous
_Z11attn_kernelPKDF16_S0_PKfS2_S2_S2_S2_PfPDF16_S3_:
	s_bfe_u32 s12, s2, 0x30003
	s_cmp_eq_u32 s12, 0
	s_cbranch_scc1 .Lsk_done
.Lsk_loop:
	s_sleep 3
	s_sub_u32 s12, s12, 1
	s_cmp_lg_u32 s12, 0
	s_cbranch_scc1 .Lsk_loop
.Lsk_done:
	s_load_dwordx8 s[4:11], s[0:1], 0x10
	v_and_b32_e32 v98, 63, v0
	v_lshlrev_b32_e32 v1, 2, v98
	s_lshr_b32 s3, s2, 4
	v_lshrrev_b32_e32 v2, 1, v0
	s_waitcnt lgkmcnt(0)
	global_load_dword v3, v1, s[4:5]
	global_load_dword v10, v1, s[6:7]
	global_load_dword v11, v1, s[8:9]
	global_load_dword v12, v1, s[10:11]
	s_load_dwordx2 s[4:5], s[0:1], 0x0
	s_lshl_b32 s6, s2, 1
	v_and_b32_e32 v1, 31, v0
	s_bfe_u32 s19, s2, 0x10003
	v_and_b32_e32 v183, 0x60, v2
	s_and_b32 s6, s6, 14
	s_lshl_b32 s16, s3, 7
	v_mov_b32_e32 v63, 0
	v_bfe_u32 v182, v0, 5, 1
	s_or_b32 s21, s6, s19
	v_or3_b32 v4, s16, v183, v1
	v_mov_b32_e32 v5, v63
	v_lshlrev_b32_e32 v62, 4, v182
	v_lshl_add_u32 v4, s21, 13, v4
	v_lshlrev_b64 v[6:7], 7, v[4:5]
	s_waitcnt lgkmcnt(0)
	v_lshl_add_u64 v[8:9], s[4:5], 0, v[62:63]
	v_add_u32_e32 v62, 0x1000, v4
	v_lshl_add_u64 v[4:5], v[8:9], 0, v[6:7]
	v_lshlrev_b64 v[6:7], 7, v[62:63]
	global_load_dwordx4 v[114:117], v[4:5], off
	global_load_dwordx4 v[118:121], v[4:5], off offset:32
	global_load_dwordx4 v[122:125], v[4:5], off offset:64
	global_load_dwordx4 v[126:129], v[4:5], off offset:96
	v_lshl_add_u64 v[4:5], v[8:9], 0, v[6:7]
	global_load_dwordx4 v[130:133], v[4:5], off
	global_load_dwordx4 v[134:137], v[4:5], off offset:32
	global_load_dwordx4 v[138:141], v[4:5], off offset:64
	global_load_dwordx4 v[142:145], v[4:5], off offset:96
	v_mbcnt_lo_u32_b32 v4, -1, 0
	v_mbcnt_hi_u32_b32 v4, -1, v4
	v_and_b32_e32 v5, 64, v4
	v_xor_b32_e32 v6, 32, v4
	v_add_u32_e32 v5, 64, v5
	v_cmp_lt_i32_e32 vcc, v6, v5
	v_xor_b32_e32 v7, 16, v4
	v_xor_b32_e32 v8, 8, v4
	v_cndmask_b32_e32 v6, v4, v6, vcc
	v_lshlrev_b32_e32 v69, 2, v6
	v_cmp_lt_i32_e32 vcc, v7, v5
	v_xor_b32_e32 v9, 4, v4
	v_xor_b32_e32 v13, 2, v4
	v_cndmask_b32_e32 v7, v4, v7, vcc
	v_lshlrev_b32_e32 v7, 2, v7
	v_cmp_lt_i32_e32 vcc, v8, v5
	v_xor_b32_e32 v14, 1, v4
	s_load_dwordx2 s[10:11], s[0:1], 0x48
	s_load_dwordx2 s[8:9], s[0:1], 0x30
	v_cndmask_b32_e32 v8, v4, v8, vcc
	v_lshlrev_b32_e32 v8, 2, v8
	v_cmp_lt_i32_e32 vcc, v9, v5
	v_readfirstlane_b32 s6, v0
	s_mov_b32 s13, 0
	v_cndmask_b32_e32 v9, v4, v9, vcc
	v_lshlrev_b32_e32 v9, 2, v9
	v_cmp_lt_i32_e32 vcc, v13, v5
	s_cmpk_lt_i32 s6, 0x100
	v_lshlrev_b32_e32 v99, 3, v182
	s_waitcnt vmcnt(10)
	v_mul_f32_e32 v6, v3, v10
	ds_bpermute_b32 v6, v69, v6
	s_waitcnt vmcnt(8)
	v_mul_f32_e32 v15, v11, v12
	ds_bpermute_b32 v15, v69, v15
	s_waitcnt lgkmcnt(0)
	v_fmac_f32_e32 v6, v3, v10
	ds_bpermute_b32 v3, v7, v6
	v_fmac_f32_e32 v15, v11, v12
	ds_bpermute_b32 v7, v7, v15
	s_waitcnt lgkmcnt(1)
	v_add_f32_e32 v3, v6, v3
	s_waitcnt lgkmcnt(0)
	v_add_f32_e32 v6, v15, v7
	ds_bpermute_b32 v7, v8, v3
	ds_bpermute_b32 v8, v8, v6
	s_waitcnt lgkmcnt(1)
	v_add_f32_e32 v3, v3, v7
	s_waitcnt lgkmcnt(0)
	v_add_f32_e32 v6, v6, v8
	ds_bpermute_b32 v7, v9, v3
	ds_bpermute_b32 v8, v9, v6
	v_cndmask_b32_e32 v9, v4, v13, vcc
	v_lshlrev_b32_e32 v180, 2, v9
	v_cmp_lt_i32_e32 vcc, v14, v5
	s_waitcnt lgkmcnt(1)
	v_add_f32_e32 v3, v3, v7
	s_waitcnt lgkmcnt(0)
	v_add_f32_e32 v6, v6, v8
	ds_bpermute_b32 v7, v180, v3
	ds_bpermute_b32 v8, v180, v6
	v_cndmask_b32_e32 v4, v4, v14, vcc
	v_lshlrev_b32_e32 v181, 2, v4
	s_waitcnt lgkmcnt(1)
	v_add_f32_e32 v78, v3, v7
	s_waitcnt lgkmcnt(0)
	v_add_f32_e32 v79, v6, v8
	ds_bpermute_b32 v80, v181, v78
	ds_bpermute_b32 v81, v181, v79
	s_cbranch_scc1 .LBB4_2
	s_setprio 1
